# conv LayerNorm and LayerNorm-2 wave sums: ds_bpermute ladders replaced by DPP adds + v_readlane (f32, order of adds differs); on top of V-loop SLP-tree removal
# speedup vs baseline: 1.0152x; 1.0014x over previous
; #define GAS __attribute__((address_space(1)))
; #define LAS __attribute__((address_space(3)))
; __device__ __forceinline__ unsigned pk2(float lo, float hi) { return f2bf(lo) | (f2bf(hi) << 16); }
; __device__ __forceinline__ void conv_phase(LAS unsigned char* lds, int tile, int tid, const bf16* __restrict__ U, const float* __restrict__ cw, const float* __restrict__ cb, ...
;     ...
;         for (int q = 0; q < 4; ++q) {
;             const int tk = wave * 4 + q;
;             const f32x4 a0 = *(const LAS f32x4*)(obuf + tk * CH + lane * 8), a1 = *(const LAS f32x4*)(obuf + tk * CH + lane * 8 + 4);
;             float v[8] = {a0.x, a0.y, a0.z, a0.w, a1.x, a1.y, a1.z, a1.w};
;             float s = 0.f;
; #pragma unroll
;             for (int e = 0; e < 8; ++e) s += v[e];
; #pragma unroll
;             for (int o = 1; o < 64; o <<= 1) s += __shfl_xor(s, o);
;             const float mean = s * (1.0f / CH); float sq = 0.f;
; #pragma unroll
;             for (int e = 0; e < 8; ++e) { v[e] -= mean; sq += v[e] * v[e]; }
; #pragma unroll
;             for (int o = 1; o < 64; o <<= 1) sq += __shfl_xor(sq, o);
;             const float rstd = 1.0f / sqrtf(sq * (1.0f / CH) + 1e-5f);
;             const f32x4 g0 = *(const GAS f32x4*)(cg + lane * 8), g1 = *(const GAS f32x4*)(cg + lane * 8 + 4), b0 = *(const GAS f32x4*)(cbeta + lane * 8), b1 = *(const GAS f32x4*)(cbeta + lane * 8 + 4);
;             const float gg[8] = {g0.x, g0.y, g0.z, g0.w, g1.x, g1.y, g1.z, g1.w}, bb[8] = {b0.x, b0.y, b0.z, b0.w, b1.x, b1.y, b1.z, b1.w};
;             float y[8];
; #pragma unroll
;             for (int e = 0; e < 8; ++e) { const float z = v[e] * rstd * gg[e] + bb[e]; y[e] = z * __builtin_amdgcn_rcpf(1.0f + __builtin_amdgcn_exp2f(-1.4426950408889634f * z)); }
;             v4u o; o.x = pk2(y[0], y[1]); o.y = pk2(y[2], y[3]); o.z = pk2(y[4], y[5]); o.w = pk2(y[6], y[7]);
;             *(GAS v4u*)(MIX + (size_t)(t0 + tk) * 1024 + 512 + lane * 8) = o;
.LBB0_374:
	v_add_u32_e32 v72, s12, v69
	ds_read_b128 v[14:17], v72
	ds_read_b128 v[72:75], v72 offset:16
	s_addk_i32 s12, 0x800
	s_cmpk_eq_i32 s12, 0x2000
	s_waitcnt lgkmcnt(1)
	v_add_f32_e32 v80, 0, v14
	v_mov_b32_e32 v76, v14
	v_add_f32_e32 v14, v15, v80
	v_add_f32_e32 v14, v16, v14
	v_add_f32_e32 v14, v17, v14
	s_waitcnt lgkmcnt(0)
	v_add_f32_e32 v14, v72, v14
	v_add_f32_e32 v14, v73, v14
	v_add_f32_e32 v14, v74, v14
	v_add_f32_e32 v14, v75, v14
	v_mov_b32_e32 v77, v16
	v_mov_b32_e32 v16, v15
	v_mov_b32_e32 v78, v72
	v_mov_b32_e32 v79, v74
	v_mov_b32_e32 v74, v73
	s_nop 1
	v_add_f32_dpp v14, v14, v14 row_shr:1 row_mask:0xf bank_mask:0xf
	s_nop 1
	v_add_f32_dpp v14, v14, v14 row_shr:2 row_mask:0xf bank_mask:0xf
	s_nop 1
	v_add_f32_dpp v14, v14, v14 row_shr:4 row_mask:0xf bank_mask:0xf
	s_nop 1
	v_add_f32_dpp v14, v14, v14 row_shr:8 row_mask:0xf bank_mask:0xf
	s_nop 1
	v_add_f32_dpp v14, v14, v14 row_bcast:15 row_mask:0xa bank_mask:0xf
	s_nop 1
	v_add_f32_dpp v14, v14, v14 row_bcast:31 row_mask:0xc bank_mask:0xf
	s_nop 1
	v_readlane_b32 s98, v14, 63
	s_nop 1
	v_mov_b32_e32 v14, s98
	v_mul_f32_e32 v14, 0x3b000000, v14
	v_pk_add_f32 v[72:73], v[76:77], v[14:15] op_sel_hi:[1,0] neg_lo:[0,1] neg_hi:[0,1]
	v_pk_add_f32 v[16:17], v[16:17], v[14:15] op_sel_hi:[1,0] neg_lo:[0,1] neg_hi:[0,1]
	v_pk_add_f32 v[76:77], v[78:79], v[14:15] op_sel_hi:[1,0] neg_lo:[0,1] neg_hi:[0,1]
	v_pk_add_f32 v[14:15], v[74:75], v[14:15] op_sel_hi:[1,0] neg_lo:[0,1] neg_hi:[0,1]
	v_pk_mul_f32 v[74:75], v[72:73], v[72:73]
	v_pk_mul_f32 v[78:79], v[16:17], v[16:17]
	v_mov_b32_e32 v80, v15
	v_add_f32_e32 v74, v74, v78
	v_add_f32_e32 v74, v75, v74
	v_add_f32_e32 v74, v79, v74
	v_mov_b32_e32 v81, v77
	v_fmac_f32_e32 v74, v76, v76
	v_pk_mul_f32 v[80:81], v[80:81], v[80:81]
	v_fmac_f32_e32 v74, v14, v14
	v_add_f32_e32 v74, v81, v74
	v_add_f32_e32 v74, v80, v74
	s_nop 1
	v_add_f32_dpp v74, v74, v74 row_shr:1 row_mask:0xf bank_mask:0xf
	s_nop 1
	v_add_f32_dpp v74, v74, v74 row_shr:2 row_mask:0xf bank_mask:0xf
	s_nop 1
	v_add_f32_dpp v74, v74, v74 row_shr:4 row_mask:0xf bank_mask:0xf
	s_nop 1
	v_add_f32_dpp v74, v74, v74 row_shr:8 row_mask:0xf bank_mask:0xf
	s_nop 1
	v_add_f32_dpp v74, v74, v74 row_bcast:15 row_mask:0xa bank_mask:0xf
	s_nop 1
	v_add_f32_dpp v74, v74, v74 row_bcast:31 row_mask:0xc bank_mask:0xf
	s_nop 1
	v_readlane_b32 s98, v74, 63
	s_nop 1
	v_mov_b32_e32 v74, s98
	v_fmamk_f32 v74, v74, 0x3b000000, v70
	v_mul_f32_e32 v75, 0x4f800000, v74
	v_cmp_gt_f32_e32 vcc, s18, v74
	s_nop 1
	v_cndmask_b32_e32 v74, v74, v75, vcc
	v_sqrt_f32_e32 v75, v74
	s_nop 0
	v_add_u32_e32 v78, -1, v75
	v_add_u32_e32 v79, 1, v75
	v_fma_f32 v80, -v78, v75, v74
	v_fma_f32 v81, -v79, v75, v74
	v_cmp_ge_f32_e64 s[6:7], 0, v80
	s_nop 1
	v_cndmask_b32_e64 v75, v75, v78, s[6:7]
	v_cmp_lt_f32_e64 s[6:7], 0, v81
	s_nop 1
	v_cndmask_b32_e64 v75, v75, v79, s[6:7]
	v_mul_f32_e32 v78, 0x37800000, v75
	v_cndmask_b32_e32 v75, v75, v78, vcc
	v_cmp_class_f32_e32 vcc, v74, v71
	s_nop 1
	v_cndmask_b32_e32 v74, v75, v74, vcc
	v_div_scale_f32 v75, s[6:7], v74, v74, 1.0
	v_rcp_f32_e32 v79, v75
	v_div_scale_f32 v78, vcc, 1.0, v74, 1.0
	v_fma_f32 v80, -v75, v79, 1.0
	v_fmac_f32_e32 v79, v80, v79
	v_mul_f32_e32 v80, v78, v79
	v_fma_f32 v81, -v75, v80, v78
	v_fmac_f32_e32 v80, v81, v79
	v_fma_f32 v75, -v75, v80, v78
	v_div_fmas_f32 v75, v75, v79, v80
	v_div_fixup_f32 v74, v75, v74, 1.0
	v_pk_mul_f32 v[72:73], v[72:73], v[74:75] op_sel_hi:[1,0]
	v_pk_mul_f32 v[16:17], v[16:17], v[74:75] op_sel_hi:[1,0]
	v_pk_mul_f32 v[76:77], v[76:77], v[74:75] op_sel_hi:[1,0]
	v_pk_mul_f32 v[14:15], v[14:15], v[74:75] op_sel_hi:[1,0]
	v_pk_fma_f32 v[72:73], v[8:9], v[72:73], v[12:13]
	v_pk_fma_f32 v[16:17], v[24:25], v[16:17], v[22:23]
	v_pk_fma_f32 v[74:75], v[0:1], v[76:77], v[4:5]
	v_pk_fma_f32 v[14:15], v[26:27], v[14:15], v[10:11]
	v_mul_f32_e32 v76, 0xbfb8aa3b, v72
	v_mul_f32_e32 v77, 0xbfb8aa3b, v16
	v_mul_f32_e32 v78, 0xbfb8aa3b, v73
	v_mul_f32_e32 v79, 0xbfb8aa3b, v17
	v_mul_f32_e32 v80, 0xbfb8aa3b, v74
	v_mul_f32_e32 v81, 0xbfb8aa3b, v14
	v_mul_f32_e32 v82, 0xbfb8aa3b, v75
	v_mul_f32_e32 v83, 0xbfb8aa3b, v15
	v_exp_f32_e32 v76, v76
	v_exp_f32_e32 v77, v77
	v_exp_f32_e32 v78, v78
	v_exp_f32_e32 v79, v79
	v_exp_f32_e32 v80, v80
	v_exp_f32_e32 v81, v81
	v_exp_f32_e32 v82, v82
	v_exp_f32_e32 v83, v83
	v_add_f32_e32 v76, 1.0, v76
	v_add_f32_e32 v77, 1.0, v77
	v_add_f32_e32 v84, 1.0, v78
	v_add_f32_e32 v79, 1.0, v79
	v_add_f32_e32 v80, 1.0, v80
	v_add_f32_e32 v81, 1.0, v81
	v_add_f32_e32 v85, 1.0, v82
	v_add_f32_e32 v83, 1.0, v83
	v_rcp_f32_e32 v76, v76
	v_rcp_f32_e32 v78, v77
	v_rcp_f32_e32 v77, v84
	v_rcp_f32_e32 v79, v79
	v_rcp_f32_e32 v80, v80
	v_rcp_f32_e32 v82, v81
	v_rcp_f32_e32 v81, v85
	v_rcp_f32_e32 v83, v83
	v_pk_mul_f32 v[72:73], v[72:73], v[76:77]
	v_pk_mul_f32 v[16:17], v[16:17], v[78:79]
	v_pk_mul_f32 v[74:75], v[74:75], v[80:81]
	v_pk_mul_f32 v[14:15], v[14:15], v[82:83]
	v_bfe_u32 v78, v17, 16, 1
	v_bfe_u32 v79, v16, 16, 1
	v_bfe_u32 v80, v72, 16, 1
	v_bfe_u32 v81, v73, 16, 1
	v_bfe_u32 v82, v74, 16, 1
	v_bfe_u32 v83, v75, 16, 1
	v_bfe_u32 v76, v15, 16, 1
	v_bfe_u32 v77, v14, 16, 1
	v_add3_u32 v79, v16, v79, s19
	v_add3_u32 v78, v17, v78, s19
	v_add3_u32 v16, v75, v83, s19
	v_add3_u32 v17, v74, v82, s19
	v_add3_u32 v73, v73, v81, s19
	v_add3_u32 v72, v72, v80, s19
	v_add3_u32 v14, v14, v77, s19
	v_add3_u32 v15, v15, v76, s19
	v_lshrrev_b32_e32 v72, 16, v72
	v_lshrrev_b32_e32 v73, 16, v73
	v_lshrrev_b32_e32 v74, 16, v17
	v_lshrrev_b32_e32 v16, 16, v16
	v_and_or_b32 v17, v15, s20, v16
	v_and_or_b32 v16, v14, s20, v74
	v_and_or_b32 v15, v78, s20, v73
	v_and_or_b32 v14, v79, s20, v72
	global_store_dwordx4 v[6:7], v[14:17], off
	v_lshl_add_u64 v[6:7], v[6:7], 0, s[8:9]
	s_cbranch_scc0 .LBB0_374
; __device__ __forceinline__ int mk_lane() { int l_ = (int)__builtin_amdgcn_mbcnt_hi(~0u, __builtin_amdgcn_mbcnt_lo(~0u, 0u)); asm volatile("" : "+v"(l_)); return l_; }
; #define BOTH(k) (IN(k) && IN((k) + 1))
; __device__ __forceinline__ void xcd_barrier_complete(unsigned* bar, unsigned x, unsigned& nloc, unsigned& nx) {
;     const unsigned G = gridDim.x * gridDim.y * gridDim.z;
;     unsigned sum, cnt, mine, sp = 0u;
;     for (;;) {
;         sum = 0u; cnt = 0u; mine = 0u;
; #pragma unroll
;         for (unsigned j = 0; j < 16; ++j) { const unsigned c = xb_ld(&bar[XB_XCNT(j)]); sum += c; cnt += (c > 0u) ? 1u : 0u; mine = (j == x) ? c : mine; }
;         if (sum == G) break;
;         __builtin_amdgcn_s_sleep(1);
;         if ((++sp & 255u) == 0u) { if (xb_ld(&bar[XB_TMO])) break; if (sp > XB_SPIN_CAP) { atomicAdd(&bar[XB_TMO], 1u); break; } }
;     }
;     nloc = mine > 0u ? mine : 1u; nx = cnt > 0u ? cnt : 1u;
; }
; __device__ __forceinline__ void xcd_barrier(const XcdBarrier& b, int wave_id, int pair = -1) {
;     asm volatile("s_waitcnt vmcnt(0)" ::: "memory");
;     __syncthreads();
;     if (wave_id == 0 && mk_lane() == 0) {
;         unsigned* bar = b.bar;
;         __builtin_amdgcn_s_waitcnt(0);
;         unsigned nloc = b.st[0], nx = b.st[1];
;         if (nloc == 0u) { xcd_barrier_complete(bar, b.x, nloc, nx); b.st[0] = nloc; b.st[1] = nx; }
; template <int K> __device__ __forceinline__ void run_phase(Frame& F, const XcdBarrier& bar, int lo, int hi, unsigned char* lds) {
;     ...
;         if (BOTH(k)) {
;             constexpr bool LOCAL_SEAM = MK_LOCALBAR && (sub == 2 || (sub == 6 && l == 0));
;             bool local = false;
;             if (LOCAL_SEAM) local = __hip_atomic_load((unsigned*)(F.ctl + CW_LBAR + 24 * 64), __ATOMIC_RELAXED, __HIP_MEMORY_SCOPE_AGENT) == 0u;
;             constexpr bool PAIR_SEAM = MK_LOCALBAR && (sub == 0 || sub == 1);
;             bool pairok = false;
;             if (PAIR_SEAM) pairok = __hip_atomic_load((unsigned*)(F.ctl + CW_LBAR + 24 * 64), __ATOMIC_RELAXED, __HIP_MEMORY_SCOPE_AGENT) == 0u;
;             if (local) xcd_local_barrier((unsigned*)(F.ctl + CW_LBAR + ((sub == 2 ? l : 2) * 8 + (bx & 7)) * 64), (unsigned)(G >> 3), (unsigned*)(F.ctl + CW_BAR) + XB_TMO, F.wave);
;             else xcd_barrier(bar, F.wave, pairok ? ((bx & 7) >> 1) : -1);
	s_mov_b32 s21, 32
	s_mov_b64 s[6:7], 0
	s_and_b64 vcc, exec, s[10:11]
	s_cbranch_vccz .LBB0_368
	s_cmp_lt_i32 s41, 4
	s_barrier
	s_cbranch_scc1 .LBB0_433
	v_mov_b32_e32 v0, 0x31000
	global_load_dword v0, v0, s[30:31] offset:2048 sc1
	s_waitcnt vmcnt(0)
	s_andn2_b64 vcc, exec, s[38:39]
	s_barrier
	s_cbranch_vccnz .LBB0_432
	s_nop 0
	v_cmp_eq_u32_e32 vcc, 0, v194
	s_and_saveexec_b64 s[6:7], vcc
	s_cbranch_execz .LBB0_431
	s_add_i32 s4, 0, 0x27f60
	v_mov_b32_e32 v1, s4
	s_waitcnt vmcnt(0) expcnt(0) lgkmcnt(0)
	ds_read_b32 v3, v1
	s_add_i32 s4, 0, 0x27f64
	v_mov_b32_e32 v1, s4
	ds_read_b32 v1, v1
	s_waitcnt lgkmcnt(1)
	v_cmp_ne_u32_e32 vcc, 0, v3
	s_cbranch_vccnz .LBB0_395
	v_readlane_b32 s4, v248, 0
	v_readlane_b32 s5, v248, 1
	s_load_dwordx2 s[10:11], s[4:5], 0x4
	s_add_u32 s4, s30, 0x4200
	s_addc_u32 s5, s31, 0
	s_add_u32 s8, s30, 0x4400
	s_addc_u32 s9, s31, 0
	s_waitcnt lgkmcnt(0)
	s_mul_i32 s58, s10, s60
	s_add_u32 s10, s30, 0x4500
	s_mul_i32 s58, s58, s11
	s_addc_u32 s11, s31, 0
	s_add_u32 s12, s30, 0x4600
	s_addc_u32 s13, s31, 0
	s_add_u32 s14, s30, 0x4700
	s_addc_u32 s15, s31, 0
	s_add_u32 s16, s30, 0x4800
	s_addc_u32 s17, s31, 0
	s_add_u32 s18, s30, 0x4900
	s_addc_u32 s19, s31, 0
	s_add_u32 s20, s30, 0x4a00
	s_addc_u32 s21, s31, 0
	s_add_u32 s22, s30, 0x4b00
	s_addc_u32 s23, s31, 0
	s_add_u32 s24, s30, 0x4c00
	s_addc_u32 s25, s31, 0
	s_add_u32 s26, s30, 0x4d00
	s_addc_u32 s27, s31, 0
	s_add_u32 s28, s30, 0x4e00
	s_addc_u32 s29, s31, 0
	s_add_u32 s42, s30, 0x4f00
	s_addc_u32 s43, s31, 0
	s_add_u32 s44, s30, 0x5000
	s_addc_u32 s45, s31, 0
	s_add_u32 s46, s30, 0x5100
	s_addc_u32 s47, s31, 0
	s_add_u32 s48, s30, 0x5200
	s_addc_u32 s49, s31, 0
	s_add_u32 s50, s30, 0x5300
	s_addc_u32 s51, s31, 0
	s_mov_b32 s59, 1
	v_mov_b32_e32 v17, 0
	s_branch .LBB0_382

; #define LAS __attribute__((address_space(3)))
; __device__ __forceinline__ void peer_ln2_phase(LAS unsigned char* lds, int wave, int blk, const bf16* __restrict__ X1B, const bf16* __restrict__ YT, const float* __restrict__ g2, const float* __restrict__ b2, ...
;     ...
;     for (int i = 0; i < 8; ++i) {
;         const int tk = wave * 8 + i; const size_t t = (size_t)blk * 64 + tk;
;         float z[16]; float s = 0.f;
; #pragma unroll
;         for (int k = 0; k < 16; ++k) { const float xv = __uint_as_float((unsigned)__builtin_nontemporal_load((const unsigned short*)X1B + t * 1024 + lane + 64 * k) << 16); const unsigned yb = *(const LAS unsigned short*)(lds + (lane + 64 * k) * 136 + tk * 2);
;             z[k] = 1.41421356237309515f * xv + __uint_as_float(yb << 16); s += z[k]; }
.LBB0_1026:
	v_lshl_add_u64 v[2:3], v[0:1], 0, s[6:7]
	v_add_u32_e32 v47, 0xfffef000, v43
	v_add_u32_e32 v48, 0xffff1200, v43
	v_add_u32_e32 v50, 0xffff5600, v43
	v_add_u32_e32 v51, 0xffff7800, v43
	v_add_u32_e32 v52, 0xffff9a00, v43
	v_add_u32_e32 v53, 0xffffbc00, v43
	v_add_u32_e32 v54, 0xffffde00, v43
	v_add_co_u32_e32 v46, vcc, 0x6000000, v2
	v_add_u32_e32 v49, 0xffff3400, v43
	ds_read_u16 v55, v43
	ds_read_u16 v56, v43 offset:8704
	ds_read_u16 v57, v43 offset:17408
	ds_read_u16 v58, v43 offset:26112
	ds_read_u16 v59, v43 offset:34816
	ds_read_u16 v60, v43 offset:43520
	ds_read_u16 v61, v43 offset:52224
	ds_read_u16 v62, v43 offset:60928
	ds_read_u16 v63, v47
	ds_read_u16 v64, v48
	ds_read_u16 v65, v49
	ds_read_u16 v50, v50
	ds_read_u16 v51, v51
	ds_read_u16 v52, v52
	ds_read_u16 v53, v53
	ds_read_u16 v54, v54
	v_add_co_u32_e64 v48, s[4:5], s10, v2
	v_addc_co_u32_e32 v47, vcc, 0, v3, vcc
	s_nop 0
	v_addc_co_u32_e64 v49, s[4:5], 0, v3, s[4:5]
	global_load_ushort v2, v[46:47], off nt
	global_load_ushort v3, v[46:47], off offset:128 nt
	global_load_ushort v66, v[46:47], off offset:256 nt
	global_load_ushort v67, v[46:47], off offset:384 nt
	global_load_ushort v68, v[46:47], off offset:512 nt
	global_load_ushort v69, v[46:47], off offset:640 nt
	global_load_ushort v70, v[46:47], off offset:768 nt
	global_load_ushort v71, v[46:47], off offset:896 nt
	global_load_ushort v72, v[46:47], off offset:1024 nt
	global_load_ushort v73, v[46:47], off offset:1152 nt
	global_load_ushort v74, v[46:47], off offset:1280 nt
	global_load_ushort v75, v[46:47], off offset:1408 nt
	global_load_ushort v76, v[46:47], off offset:1536 nt
	global_load_ushort v77, v[46:47], off offset:1664 nt
	global_load_ushort v78, v[46:47], off offset:1792 nt
	s_nop 0
	global_load_ushort v46, v[46:47], off offset:1920 nt
	s_waitcnt lgkmcnt(14)
	v_lshlrev_b32_e32 v47, 16, v55
	v_lshlrev_b32_e32 v55, 16, v56
	s_waitcnt lgkmcnt(13)
	v_lshlrev_b32_e32 v56, 16, v57
	s_waitcnt lgkmcnt(12)
	v_lshlrev_b32_e32 v57, 16, v58
	s_waitcnt lgkmcnt(11)
	v_lshlrev_b32_e32 v58, 16, v59
	s_waitcnt lgkmcnt(10)
	v_lshlrev_b32_e32 v59, 16, v60
	s_waitcnt lgkmcnt(9)
	v_lshlrev_b32_e32 v60, 16, v61
	s_waitcnt lgkmcnt(8)
	v_lshlrev_b32_e32 v61, 16, v62
	s_waitcnt lgkmcnt(7)
	v_lshlrev_b32_e32 v62, 16, v63
	s_waitcnt lgkmcnt(6)
	v_lshlrev_b32_e32 v63, 16, v64
	s_waitcnt lgkmcnt(5)
	v_lshlrev_b32_e32 v64, 16, v65
	s_waitcnt lgkmcnt(4)
	v_lshlrev_b32_e32 v50, 16, v50
	s_waitcnt lgkmcnt(3)
	v_lshlrev_b32_e32 v51, 16, v51
	s_waitcnt lgkmcnt(2)
	v_lshlrev_b32_e32 v52, 16, v52
	s_waitcnt lgkmcnt(1)
	v_lshlrev_b32_e32 v53, 16, v53
	s_waitcnt lgkmcnt(0)
	v_lshlrev_b32_e32 v54, 16, v54
	s_add_u32 s6, s6, 0x800
	s_addc_u32 s7, s7, 0
	v_add_u32_e32 v43, 2, v43
	s_cmpk_lg_i32 s6, 0x4000
	s_waitcnt vmcnt(15)
	v_lshlrev_b32_e32 v2, 16, v2
	s_waitcnt vmcnt(14)
	v_lshlrev_b32_e32 v3, 16, v3
	v_fmac_f32_e32 v62, 0x3fb504f3, v2
	s_waitcnt vmcnt(13)
	v_lshlrev_b32_e32 v65, 16, v66
	v_fmac_f32_e32 v63, 0x3fb504f3, v3
	v_add_f32_e32 v2, 0, v62
	s_waitcnt vmcnt(12)
	v_lshlrev_b32_e32 v66, 16, v67
	v_fmac_f32_e32 v64, 0x3fb504f3, v65
	v_add_f32_e32 v2, v2, v63
	s_waitcnt vmcnt(11)
	v_lshlrev_b32_e32 v67, 16, v68
	v_fmac_f32_e32 v50, 0x3fb504f3, v66
	v_add_f32_e32 v2, v2, v64
	s_waitcnt vmcnt(10)
	v_lshlrev_b32_e32 v68, 16, v69
	v_fmac_f32_e32 v51, 0x3fb504f3, v67
	v_add_f32_e32 v2, v2, v50
	s_waitcnt vmcnt(9)
	v_lshlrev_b32_e32 v69, 16, v70
	v_fmac_f32_e32 v52, 0x3fb504f3, v68
	v_add_f32_e32 v2, v2, v51
	s_waitcnt vmcnt(8)
	v_lshlrev_b32_e32 v70, 16, v71
	v_fmac_f32_e32 v53, 0x3fb504f3, v69
	v_add_f32_e32 v2, v2, v52
	s_waitcnt vmcnt(7)
	v_lshlrev_b32_e32 v71, 16, v72
	v_fmac_f32_e32 v54, 0x3fb504f3, v70
	v_add_f32_e32 v2, v2, v53
	s_waitcnt vmcnt(6)
	v_lshlrev_b32_e32 v72, 16, v73
	v_fmac_f32_e32 v47, 0x3fb504f3, v71
	v_add_f32_e32 v2, v2, v54
	s_waitcnt vmcnt(5)
	v_lshlrev_b32_e32 v73, 16, v74
	v_fmac_f32_e32 v55, 0x3fb504f3, v72
	v_add_f32_e32 v2, v2, v47
	s_waitcnt vmcnt(4)
	v_lshlrev_b32_e32 v74, 16, v75
	v_fmac_f32_e32 v56, 0x3fb504f3, v73
	v_add_f32_e32 v2, v2, v55
	s_waitcnt vmcnt(3)
	v_lshlrev_b32_e32 v75, 16, v76
	v_fmac_f32_e32 v57, 0x3fb504f3, v74
	v_add_f32_e32 v2, v2, v56
	s_waitcnt vmcnt(2)
	v_lshlrev_b32_e32 v76, 16, v77
	v_fmac_f32_e32 v58, 0x3fb504f3, v75
	v_add_f32_e32 v2, v2, v57
	s_waitcnt vmcnt(1)
	v_lshlrev_b32_e32 v77, 16, v78
	v_fmac_f32_e32 v59, 0x3fb504f3, v76
	v_add_f32_e32 v2, v2, v58
	s_waitcnt vmcnt(0)
; #define GAS __attribute__((address_space(1)))
; __device__ __forceinline__ unsigned f2bf(float f) { unsigned u = __builtin_bit_cast(unsigned, f); return (u + 0x7fffu + ((u >> 16) & 1u)) >> 16; }
; __device__ __forceinline__ void peer_ln2_phase(LAS unsigned char* lds, int wave, int blk, const bf16* __restrict__ X1B, const bf16* __restrict__ YT, const float* __restrict__ g2, const float* __restrict__ b2, ...
;     ...
; #pragma unroll
;         for (int o = 1; o < 64; o <<= 1) s += __shfl_xor(s, o);
;         const float mean = s * (1.0f / 1024.0f); float sq = 0.f;
; #pragma unroll
;         for (int k = 0; k < 16; ++k) { z[k] -= mean; sq += z[k] * z[k]; }
; #pragma unroll
;         for (int o = 1; o < 64; o <<= 1) sq += __shfl_xor(sq, o);
;         const float rstd = 1.0f / sqrtf(sq * (1.0f / 1024.0f) + 1e-5f);
; #pragma unroll
;         for (int k = 0; k < 16; ++k) { z[k] = z[k] * rstd * gv[k] + bv[k]; if (outf) __builtin_nontemporal_store(z[k], outf + t * 1024 + lane + 64 * k); }
;         if (outb) {
; #pragma unroll
;             for (int k = 0; k < 16; ++k) ((GAS unsigned short*)outb)[t * 1024 + lane + 64 * k] = (unsigned short)f2bf(z[k]); }
	v_lshlrev_b32_e32 v46, 16, v46
	v_fmac_f32_e32 v60, 0x3fb504f3, v77
	v_add_f32_e32 v2, v2, v59
	v_fmac_f32_e32 v61, 0x3fb504f3, v46
	v_add_f32_e32 v2, v2, v60
	v_add_f32_e32 v2, v2, v61
	s_nop 1
	v_add_f32_dpp v2, v2, v2 row_shr:1 row_mask:0xf bank_mask:0xf
	s_nop 1
	v_add_f32_dpp v2, v2, v2 row_shr:2 row_mask:0xf bank_mask:0xf
	s_nop 1
	v_add_f32_dpp v2, v2, v2 row_shr:4 row_mask:0xf bank_mask:0xf
	s_nop 1
	v_add_f32_dpp v2, v2, v2 row_shr:8 row_mask:0xf bank_mask:0xf
	s_nop 1
	v_add_f32_dpp v2, v2, v2 row_bcast:15 row_mask:0xa bank_mask:0xf
	s_nop 1
	v_add_f32_dpp v2, v2, v2 row_bcast:31 row_mask:0xc bank_mask:0xf
	s_nop 1
	v_readlane_b32 s98, v2, 63
	s_nop 1
	v_mov_b32_e32 v2, s98
	v_fmac_f32_e32 v63, 0xba800000, v2
	v_fmac_f32_e32 v62, 0xba800000, v2
	v_fmac_f32_e32 v64, 0xba800000, v2
	v_fmac_f32_e32 v50, 0xba800000, v2
	v_fmac_f32_e32 v51, 0xba800000, v2
	v_fmac_f32_e32 v52, 0xba800000, v2
	v_fmac_f32_e32 v53, 0xba800000, v2
	v_fmac_f32_e32 v54, 0xba800000, v2
	v_fmac_f32_e32 v47, 0xba800000, v2
	v_fmac_f32_e32 v55, 0xba800000, v2
	v_fmac_f32_e32 v56, 0xba800000, v2
	v_fmac_f32_e32 v57, 0xba800000, v2
	v_fmac_f32_e32 v58, 0xba800000, v2
	v_fmac_f32_e32 v59, 0xba800000, v2
	v_fmac_f32_e32 v60, 0xba800000, v2
	v_fmac_f32_e32 v61, 0xba800000, v2
	v_mul_f32_e32 v2, v63, v63
	v_fmac_f32_e32 v2, v62, v62
	v_fmac_f32_e32 v2, v64, v64
	v_fmac_f32_e32 v2, v50, v50
	v_fmac_f32_e32 v2, v51, v51
	v_fmac_f32_e32 v2, v52, v52
	v_fmac_f32_e32 v2, v53, v53
	v_fmac_f32_e32 v2, v54, v54
	v_fmac_f32_e32 v2, v47, v47
	v_fmac_f32_e32 v2, v55, v55
	v_fmac_f32_e32 v2, v56, v56
	v_fmac_f32_e32 v2, v57, v57
	v_fmac_f32_e32 v2, v58, v58
	v_fmac_f32_e32 v2, v59, v59
	v_fmac_f32_e32 v2, v60, v60
	v_fmac_f32_e32 v2, v61, v61
	s_nop 1
	v_add_f32_dpp v2, v2, v2 row_shr:1 row_mask:0xf bank_mask:0xf
	s_nop 1
	v_add_f32_dpp v2, v2, v2 row_shr:2 row_mask:0xf bank_mask:0xf
	s_nop 1
	v_add_f32_dpp v2, v2, v2 row_shr:4 row_mask:0xf bank_mask:0xf
	s_nop 1
	v_add_f32_dpp v2, v2, v2 row_shr:8 row_mask:0xf bank_mask:0xf
	s_nop 1
	v_add_f32_dpp v2, v2, v2 row_bcast:15 row_mask:0xa bank_mask:0xf
	s_nop 1
	v_add_f32_dpp v2, v2, v2 row_bcast:31 row_mask:0xc bank_mask:0xf
	s_nop 1
	v_readlane_b32 s98, v2, 63
	s_nop 1
	v_mov_b32_e32 v2, s98
	v_fmamk_f32 v2, v2, 0x3a800000, v44
	v_mul_f32_e32 v3, 0x4f800000, v2
	v_cmp_gt_f32_e32 vcc, s8, v2
	s_nop 1
	v_cndmask_b32_e32 v2, v2, v3, vcc
	v_sqrt_f32_e32 v3, v2
	s_nop 0
	v_add_u32_e32 v46, -1, v3
	v_add_u32_e32 v65, 1, v3
	v_fma_f32 v66, -v46, v3, v2
	v_fma_f32 v67, -v65, v3, v2
	v_cmp_ge_f32_e64 s[4:5], 0, v66
	s_nop 1
	v_cndmask_b32_e64 v3, v3, v46, s[4:5]
	v_cmp_lt_f32_e64 s[4:5], 0, v67
	s_nop 1
	v_cndmask_b32_e64 v3, v3, v65, s[4:5]
	v_mul_f32_e32 v46, 0x37800000, v3
	v_cndmask_b32_e32 v3, v3, v46, vcc
	v_cmp_class_f32_e32 vcc, v2, v45
	s_nop 1
	v_cndmask_b32_e32 v2, v3, v2, vcc
	v_div_scale_f32 v3, s[4:5], v2, v2, 1.0
	v_rcp_f32_e32 v65, v3
	v_div_scale_f32 v46, vcc, 1.0, v2, 1.0
	v_fma_f32 v66, -v3, v65, 1.0
	v_fmac_f32_e32 v65, v66, v65
	v_mul_f32_e32 v66, v46, v65
	v_fma_f32 v67, -v3, v66, v46
	v_fmac_f32_e32 v66, v67, v65
	v_fma_f32 v3, -v3, v66, v46
	v_div_fmas_f32 v3, v3, v65, v66
	v_div_fixup_f32 v2, v3, v2, 1.0
	v_mul_f32_e32 v3, v62, v2
	v_mul_f32_e32 v46, v63, v2
	v_mul_f32_e32 v62, v64, v2
	v_mul_f32_e32 v50, v50, v2
	v_mul_f32_e32 v51, v51, v2
	v_mul_f32_e32 v52, v52, v2
	v_mul_f32_e32 v53, v53, v2
	v_mul_f32_e32 v54, v54, v2
	v_mul_f32_e32 v47, v47, v2
	v_mul_f32_e32 v55, v55, v2
	v_mul_f32_e32 v56, v56, v2
	v_mul_f32_e32 v57, v57, v2
	v_mul_f32_e32 v58, v58, v2
	v_mul_f32_e32 v59, v59, v2
	v_mul_f32_e32 v60, v60, v2
	v_mul_f32_e32 v2, v61, v2
	v_fma_f32 v3, v4, v3, v13
	v_fma_f32 v46, v5, v46, v14
	v_fma_f32 v61, v6, v62, v15
	v_fma_f32 v50, v7, v50, v16
	v_fma_f32 v51, v9, v51, v17
	v_fma_f32 v52, v10, v52, v18
	v_fma_f32 v53, v11, v53, v19
	v_fma_f32 v54, v12, v54, v20
	v_fma_f32 v47, v21, v47, v29
	v_fma_f32 v55, v22, v55, v30
	v_fma_f32 v56, v23, v56, v31
	v_fma_f32 v57, v24, v57, v32
	v_fma_f32 v58, v25, v58, v33
	v_fma_f32 v59, v26, v59, v34
	v_fma_f32 v60, v27, v60, v35
	v_fma_f32 v2, v28, v2, v36
	v_bfe_u32 v62, v3, 16, 1
	v_bfe_u32 v63, v46, 16, 1
	v_bfe_u32 v64, v61, 16, 1
	v_bfe_u32 v65, v50, 16, 1
	v_bfe_u32 v66, v51, 16, 1
	v_bfe_u32 v67, v52, 16, 1
	v_bfe_u32 v68, v53, 16, 1
	v_bfe_u32 v69, v54, 16, 1
	v_bfe_u32 v70, v47, 16, 1
	v_bfe_u32 v71, v55, 16, 1
	v_bfe_u32 v72, v56, 16, 1
	v_bfe_u32 v73, v57, 16, 1
	v_bfe_u32 v74, v58, 16, 1
	v_bfe_u32 v75, v59, 16, 1
	v_bfe_u32 v76, v60, 16, 1
	v_bfe_u32 v77, v2, 16, 1
	v_add3_u32 v3, v3, v62, s9
	v_add3_u32 v46, v46, v63, s9
	v_add3_u32 v61, v61, v64, s9
	v_add3_u32 v50, v50, v65, s9
	v_add3_u32 v51, v51, v66, s9
	v_add3_u32 v52, v52, v67, s9
	v_add3_u32 v53, v53, v68, s9
	v_add3_u32 v54, v54, v69, s9
	v_add3_u32 v47, v47, v70, s9
	v_add3_u32 v55, v55, v71, s9
	v_add3_u32 v56, v56, v72, s9
	v_add3_u32 v57, v57, v73, s9
	v_add3_u32 v58, v58, v74, s9
	v_add3_u32 v59, v59, v75, s9
	v_add3_u32 v60, v60, v76, s9
	v_add3_u32 v2, v2, v77, s9
	global_store_short_d16_hi v[48:49], v3, off
	global_store_short_d16_hi v[48:49], v46, off offset:128
	global_store_short_d16_hi v[48:49], v61, off offset:256
	global_store_short_d16_hi v[48:49], v50, off offset:384
	global_store_short_d16_hi v[48:49], v51, off offset:512
	global_store_short_d16_hi v[48:49], v52, off offset:640
	global_store_short_d16_hi v[48:49], v53, off offset:768
	global_store_short_d16_hi v[48:49], v54, off offset:896
	global_store_short_d16_hi v[48:49], v47, off offset:1024
	global_store_short_d16_hi v[48:49], v55, off offset:1152
	global_store_short_d16_hi v[48:49], v56, off offset:1280
	global_store_short_d16_hi v[48:49], v57, off offset:1408
	global_store_short_d16_hi v[48:49], v58, off offset:1536
	global_store_short_d16_hi v[48:49], v59, off offset:1664
	global_store_short_d16_hi v[48:49], v60, off offset:1792
	global_store_short_d16_hi v[48:49], v2, off offset:1920
	s_cbranch_scc1 .LBB0_1026
; __device__ __forceinline__ int mk_lane() { int l_ = (int)__builtin_amdgcn_mbcnt_hi(~0u, __builtin_amdgcn_mbcnt_lo(~0u, 0u)); asm volatile("" : "+v"(l_)); return l_; }
; #define BOTH(k) (IN(k) && IN((k) + 1))
; __device__ __forceinline__ void xcd_barrier_complete(unsigned* bar, unsigned x, unsigned& nloc, unsigned& nx) {
;     const unsigned G = gridDim.x * gridDim.y * gridDim.z;
;     unsigned sum, cnt, mine, sp = 0u;
;     for (;;) {
;         sum = 0u; cnt = 0u; mine = 0u;
; #pragma unroll
;         for (unsigned j = 0; j < 16; ++j) { const unsigned c = xb_ld(&bar[XB_XCNT(j)]); sum += c; cnt += (c > 0u) ? 1u : 0u; mine = (j == x) ? c : mine; }
;         if (sum == G) break;
;         __builtin_amdgcn_s_sleep(1);
;         if ((++sp & 255u) == 0u) { if (xb_ld(&bar[XB_TMO])) break; if (sp > XB_SPIN_CAP) { atomicAdd(&bar[XB_TMO], 1u); break; } }
;     }
;     nloc = mine > 0u ? mine : 1u; nx = cnt > 0u ? cnt : 1u;
; }
; __device__ __forceinline__ void xcd_barrier(const XcdBarrier& b, int wave_id, int pair = -1) {
;     asm volatile("s_waitcnt vmcnt(0)" ::: "memory");
;     __syncthreads();
;     if (wave_id == 0 && mk_lane() == 0) {
;         unsigned* bar = b.bar;
;         __builtin_amdgcn_s_waitcnt(0);
;         unsigned nloc = b.st[0], nx = b.st[1];
;         if (nloc == 0u) { xcd_barrier_complete(bar, b.x, nloc, nx); b.st[0] = nloc; b.st[1] = nx; }
; template <int K> __device__ __forceinline__ void run_phase(Frame& F, const XcdBarrier& bar, int lo, int hi, unsigned char* lds) {
;     ...
;         if (BOTH(k)) {
;             constexpr bool LOCAL_SEAM = MK_LOCALBAR && (sub == 2 || (sub == 6 && l == 0));
;             bool local = false;
;             if (LOCAL_SEAM) local = __hip_atomic_load((unsigned*)(F.ctl + CW_LBAR + 24 * 64), __ATOMIC_RELAXED, __HIP_MEMORY_SCOPE_AGENT) == 0u;
;             constexpr bool PAIR_SEAM = MK_LOCALBAR && (sub == 0 || sub == 1);
;             bool pairok = false;
;             if (PAIR_SEAM) pairok = __hip_atomic_load((unsigned*)(F.ctl + CW_LBAR + 24 * 64), __ATOMIC_RELAXED, __HIP_MEMORY_SCOPE_AGENT) == 0u;
;             if (local) xcd_local_barrier((unsigned*)(F.ctl + CW_LBAR + ((sub == 2 ? l : 2) * 8 + (bx & 7)) * 64), (unsigned)(G >> 3), (unsigned*)(F.ctl + CW_BAR) + XB_TMO, F.wave);
;             else xcd_barrier(bar, F.wave, pairok ? ((bx & 7) >> 1) : -1);
	s_cmp_lt_u32 s41, 9
	s_barrier
	s_cbranch_scc1 .LBB0_1106
	v_mov_b32_e32 v0, 0x31000
	global_load_dword v0, v0, s[30:31] offset:2048 sc1
	s_waitcnt vmcnt(0)
	v_cmp_ne_u32_e32 vcc, 0, v0
	s_cbranch_vccz .LBB0_1041
	s_waitcnt vmcnt(0)
	s_andn2_b64 vcc, exec, s[38:39]
	s_barrier
	s_cbranch_vccnz .LBB0_1084
	v_mov_b32_e32 v0, v8
	s_nop 0
	v_cmp_eq_u32_e32 vcc, 0, v0
	s_and_saveexec_b64 s[4:5], vcc
	s_cbranch_execz .LBB0_1083
	s_add_i32 s6, 0, 0x27f60
	v_mov_b32_e32 v0, s6
	s_waitcnt vmcnt(0) expcnt(0) lgkmcnt(0)
	ds_read_b32 v2, v0
	s_add_i32 s6, 0, 0x27f64
	v_mov_b32_e32 v0, s6
	ds_read_b32 v0, v0
	s_waitcnt lgkmcnt(1)
	v_cmp_ne_u32_e32 vcc, 0, v2
	s_cbranch_vccnz .LBB0_1047
	v_readlane_b32 s6, v248, 0
	v_readlane_b32 s7, v248, 1
	s_load_dwordx2 s[10:11], s[6:7], 0x4
	s_add_u32 s6, s30, 0x4200
	s_addc_u32 s7, s31, 0
	s_add_u32 s8, s30, 0x4400
	s_addc_u32 s9, s31, 0
	s_waitcnt lgkmcnt(0)
	s_mul_i32 s59, s10, s60
	s_add_u32 s10, s30, 0x4500
	s_mul_i32 s59, s59, s11
	s_addc_u32 s11, s31, 0
	s_add_u32 s12, s30, 0x4600
	s_addc_u32 s13, s31, 0
	s_add_u32 s14, s30, 0x4700
	s_addc_u32 s15, s31, 0
	s_add_u32 s16, s30, 0x4800
	s_addc_u32 s17, s31, 0
	s_add_u32 s18, s30, 0x4900
	s_addc_u32 s19, s31, 0
	s_add_u32 s20, s30, 0x4a00
	s_addc_u32 s21, s31, 0
	s_add_u32 s22, s30, 0x4b00
	s_addc_u32 s23, s31, 0
	s_add_u32 s24, s30, 0x4c00
	s_addc_u32 s25, s31, 0
	s_add_u32 s26, s30, 0x4d00
	s_addc_u32 s27, s31, 0
	s_add_u32 s28, s30, 0x4e00
	s_addc_u32 s29, s31, 0
	s_add_u32 s42, s30, 0x4f00
	s_addc_u32 s43, s31, 0
	s_add_u32 s44, s30, 0x5000
	s_addc_u32 s45, s31, 0
	s_add_u32 s46, s30, 0x5100
	s_addc_u32 s47, s31, 0
	s_add_u32 s48, s30, 0x5200
	s_addc_u32 s49, s31, 0
	s_add_u32 s50, s30, 0x5300
	s_addc_u32 s51, s31, 0
	s_mov_b32 s62, 1
	v_mov_b32_e32 v17, 0
	s_branch .LBB0_1034

; #define GAS __attribute__((address_space(1)))
; #define LAS __attribute__((address_space(3)))
; __device__ __forceinline__ unsigned pk2(float lo, float hi) { return f2bf(lo) | (f2bf(hi) << 16); }
; __device__ __forceinline__ void conv_phase(LAS unsigned char* lds, int tile, int tid, const bf16* __restrict__ U, const float* __restrict__ cw, const float* __restrict__ cb, ...
;     ...
;         for (int q = 0; q < 4; ++q) {
;             const int tk = wave * 4 + q;
;             const f32x4 a0 = *(const LAS f32x4*)(obuf + tk * CH + lane * 8), a1 = *(const LAS f32x4*)(obuf + tk * CH + lane * 8 + 4);
;             float v[8] = {a0.x, a0.y, a0.z, a0.w, a1.x, a1.y, a1.z, a1.w};
;             float s = 0.f;
; #pragma unroll
;             for (int e = 0; e < 8; ++e) s += v[e];
; #pragma unroll
;             for (int o = 1; o < 64; o <<= 1) s += __shfl_xor(s, o);
;             const float mean = s * (1.0f / CH); float sq = 0.f;
; #pragma unroll
;             for (int e = 0; e < 8; ++e) { v[e] -= mean; sq += v[e] * v[e]; }
; #pragma unroll
;             for (int o = 1; o < 64; o <<= 1) sq += __shfl_xor(sq, o);
;             const float rstd = 1.0f / sqrtf(sq * (1.0f / CH) + 1e-5f);
;             const f32x4 g0 = *(const GAS f32x4*)(cg + lane * 8), g1 = *(const GAS f32x4*)(cg + lane * 8 + 4), b0 = *(const GAS f32x4*)(cbeta + lane * 8), b1 = *(const GAS f32x4*)(cbeta + lane * 8 + 4);
;             const float gg[8] = {g0.x, g0.y, g0.z, g0.w, g1.x, g1.y, g1.z, g1.w}, bb[8] = {b0.x, b0.y, b0.z, b0.w, b1.x, b1.y, b1.z, b1.w};
;             float y[8];
; #pragma unroll
;             for (int e = 0; e < 8; ++e) { const float z = v[e] * rstd * gg[e] + bb[e]; y[e] = z * __builtin_amdgcn_rcpf(1.0f + __builtin_amdgcn_exp2f(-1.4426950408889634f * z)); }
;             v4u o; o.x = pk2(y[0], y[1]); o.y = pk2(y[2], y[3]); o.z = pk2(y[4], y[5]); o.w = pk2(y[6], y[7]);
;             *(GAS v4u*)(MIX + (size_t)(t0 + tk) * 1024 + 512 + lane * 8) = o;
.LBB0_1370:
	v_add_u32_e32 v16, s12, v67
	ds_read_b128 v[70:73], v16
	ds_read_b128 v[74:77], v16 offset:16
	s_addk_i32 s12, 0x800
	s_cmpk_eq_i32 s12, 0x2000
	s_waitcnt lgkmcnt(1)
	v_add_f32_e32 v80, 0, v70
	v_mov_b32_e32 v16, v70
	v_add_f32_e32 v70, v71, v80
	v_add_f32_e32 v70, v72, v70
	v_add_f32_e32 v70, v73, v70
	s_waitcnt lgkmcnt(0)
	v_add_f32_e32 v70, v74, v70
	v_add_f32_e32 v70, v75, v70
	v_add_f32_e32 v70, v76, v70
	v_add_f32_e32 v70, v77, v70
	v_mov_b32_e32 v17, v72
	v_mov_b32_e32 v72, v71
	v_mov_b32_e32 v78, v74
	v_mov_b32_e32 v79, v76
	v_mov_b32_e32 v76, v75
	s_nop 1
	v_add_f32_dpp v70, v70, v70 row_shr:1 row_mask:0xf bank_mask:0xf
	s_nop 1
	v_add_f32_dpp v70, v70, v70 row_shr:2 row_mask:0xf bank_mask:0xf
	s_nop 1
	v_add_f32_dpp v70, v70, v70 row_shr:4 row_mask:0xf bank_mask:0xf
	s_nop 1
	v_add_f32_dpp v70, v70, v70 row_shr:8 row_mask:0xf bank_mask:0xf
	s_nop 1
	v_add_f32_dpp v70, v70, v70 row_bcast:15 row_mask:0xa bank_mask:0xf
	s_nop 1
	v_add_f32_dpp v70, v70, v70 row_bcast:31 row_mask:0xc bank_mask:0xf
	s_nop 1
	v_readlane_b32 s98, v70, 63
	s_nop 1
	v_mov_b32_e32 v70, s98
	v_mul_f32_e32 v70, 0x3b000000, v70
	v_pk_add_f32 v[16:17], v[16:17], v[70:71] op_sel_hi:[1,0] neg_lo:[0,1] neg_hi:[0,1]
	v_pk_add_f32 v[72:73], v[72:73], v[70:71] op_sel_hi:[1,0] neg_lo:[0,1] neg_hi:[0,1]
	v_pk_add_f32 v[74:75], v[78:79], v[70:71] op_sel_hi:[1,0] neg_lo:[0,1] neg_hi:[0,1]
	v_pk_add_f32 v[70:71], v[76:77], v[70:71] op_sel_hi:[1,0] neg_lo:[0,1] neg_hi:[0,1]
	v_pk_mul_f32 v[76:77], v[16:17], v[16:17]
	v_pk_mul_f32 v[78:79], v[72:73], v[72:73]
	v_mov_b32_e32 v80, v71
	v_add_f32_e32 v76, v76, v78
	v_add_f32_e32 v76, v77, v76
	v_add_f32_e32 v76, v79, v76
	v_mov_b32_e32 v81, v75
	v_fmac_f32_e32 v76, v74, v74
	v_pk_mul_f32 v[80:81], v[80:81], v[80:81]
	v_fmac_f32_e32 v76, v70, v70
	v_add_f32_e32 v76, v81, v76
	v_add_f32_e32 v76, v80, v76
	s_nop 1
	v_add_f32_dpp v76, v76, v76 row_shr:1 row_mask:0xf bank_mask:0xf
	s_nop 1
	v_add_f32_dpp v76, v76, v76 row_shr:2 row_mask:0xf bank_mask:0xf
	s_nop 1
	v_add_f32_dpp v76, v76, v76 row_shr:4 row_mask:0xf bank_mask:0xf
	s_nop 1
	v_add_f32_dpp v76, v76, v76 row_shr:8 row_mask:0xf bank_mask:0xf
	s_nop 1
	v_add_f32_dpp v76, v76, v76 row_bcast:15 row_mask:0xa bank_mask:0xf
	s_nop 1
	v_add_f32_dpp v76, v76, v76 row_bcast:31 row_mask:0xc bank_mask:0xf
	s_nop 1
	v_readlane_b32 s98, v76, 63
	s_nop 1
	v_mov_b32_e32 v76, s98
	v_fmamk_f32 v76, v76, 0x3b000000, v68
	v_mul_f32_e32 v77, 0x4f800000, v76
	v_cmp_gt_f32_e32 vcc, s18, v76
	s_nop 1
	v_cndmask_b32_e32 v76, v76, v77, vcc
	v_sqrt_f32_e32 v77, v76
	s_nop 0
	v_add_u32_e32 v78, -1, v77
	v_add_u32_e32 v79, 1, v77
	v_fma_f32 v80, -v78, v77, v76
	v_fma_f32 v81, -v79, v77, v76
	v_cmp_ge_f32_e64 s[6:7], 0, v80
	s_nop 1
	v_cndmask_b32_e64 v77, v77, v78, s[6:7]
	v_cmp_lt_f32_e64 s[6:7], 0, v81
	s_nop 1
	v_cndmask_b32_e64 v77, v77, v79, s[6:7]
	v_mul_f32_e32 v78, 0x37800000, v77
	v_cndmask_b32_e32 v77, v77, v78, vcc
	v_cmp_class_f32_e32 vcc, v76, v69
	s_nop 1
	v_cndmask_b32_e32 v76, v77, v76, vcc
	v_div_scale_f32 v77, s[6:7], v76, v76, 1.0
	v_rcp_f32_e32 v79, v77
	v_div_scale_f32 v78, vcc, 1.0, v76, 1.0
	v_fma_f32 v80, -v77, v79, 1.0
	v_fmac_f32_e32 v79, v80, v79
	v_mul_f32_e32 v80, v78, v79
	v_fma_f32 v81, -v77, v80, v78
	v_fmac_f32_e32 v80, v81, v79
	v_fma_f32 v77, -v77, v80, v78
	v_div_fmas_f32 v77, v77, v79, v80
	v_div_fixup_f32 v76, v77, v76, 1.0
	v_pk_mul_f32 v[16:17], v[16:17], v[76:77] op_sel_hi:[1,0]
	v_pk_mul_f32 v[72:73], v[72:73], v[76:77] op_sel_hi:[1,0]
	v_pk_mul_f32 v[74:75], v[74:75], v[76:77] op_sel_hi:[1,0]
	v_pk_mul_f32 v[70:71], v[70:71], v[76:77] op_sel_hi:[1,0]
	v_pk_fma_f32 v[16:17], v[0:1], v[16:17], v[4:5]
	v_pk_fma_f32 v[72:73], v[24:25], v[72:73], v[22:23]
	v_pk_fma_f32 v[74:75], v[8:9], v[74:75], v[12:13]
	v_pk_fma_f32 v[70:71], v[6:7], v[70:71], v[2:3]
	v_mul_f32_e32 v76, 0xbfb8aa3b, v16
	v_mul_f32_e32 v77, 0xbfb8aa3b, v72
	v_mul_f32_e32 v78, 0xbfb8aa3b, v17
	v_mul_f32_e32 v79, 0xbfb8aa3b, v73
	v_mul_f32_e32 v80, 0xbfb8aa3b, v74
	v_mul_f32_e32 v81, 0xbfb8aa3b, v70
	v_mul_f32_e32 v82, 0xbfb8aa3b, v75
	v_mul_f32_e32 v83, 0xbfb8aa3b, v71
	v_exp_f32_e32 v76, v76
	v_exp_f32_e32 v77, v77
	v_exp_f32_e32 v78, v78
	v_exp_f32_e32 v79, v79
	v_exp_f32_e32 v80, v80
	v_exp_f32_e32 v81, v81
	v_exp_f32_e32 v82, v82
	v_exp_f32_e32 v83, v83
	v_add_f32_e32 v76, 1.0, v76
	v_add_f32_e32 v77, 1.0, v77
	v_add_f32_e32 v84, 1.0, v78
	v_add_f32_e32 v79, 1.0, v79
	v_add_f32_e32 v80, 1.0, v80
	v_add_f32_e32 v81, 1.0, v81
	v_add_f32_e32 v85, 1.0, v82
	v_add_f32_e32 v83, 1.0, v83
	v_rcp_f32_e32 v76, v76
	v_rcp_f32_e32 v78, v77
	v_rcp_f32_e32 v77, v84
	v_rcp_f32_e32 v79, v79
	v_rcp_f32_e32 v80, v80
	v_rcp_f32_e32 v82, v81
	v_rcp_f32_e32 v81, v85
	v_rcp_f32_e32 v83, v83
	v_pk_mul_f32 v[16:17], v[16:17], v[76:77]
	v_pk_mul_f32 v[72:73], v[72:73], v[78:79]
	v_pk_mul_f32 v[74:75], v[74:75], v[80:81]
	v_pk_mul_f32 v[70:71], v[70:71], v[82:83]
	v_bfe_u32 v78, v73, 16, 1
	v_bfe_u32 v79, v72, 16, 1
	v_bfe_u32 v80, v16, 16, 1
	v_bfe_u32 v81, v17, 16, 1
	v_bfe_u32 v82, v74, 16, 1
	v_bfe_u32 v83, v75, 16, 1
	v_bfe_u32 v76, v71, 16, 1
	v_bfe_u32 v77, v70, 16, 1
	v_add3_u32 v79, v72, v79, s19
	v_add3_u32 v78, v73, v78, s19
	v_add3_u32 v72, v75, v83, s19
	v_add3_u32 v73, v74, v82, s19
	v_add3_u32 v17, v17, v81, s19
	v_add3_u32 v16, v16, v80, s19
	v_add3_u32 v70, v70, v77, s19
	v_add3_u32 v71, v71, v76, s19
	v_lshrrev_b32_e32 v16, 16, v16
	v_lshrrev_b32_e32 v17, 16, v17
	v_lshrrev_b32_e32 v74, 16, v73
	v_lshrrev_b32_e32 v72, 16, v72
	v_and_or_b32 v73, v71, s20, v72
	v_and_or_b32 v72, v70, s20, v74
	v_and_or_b32 v71, v78, s20, v17
	v_and_or_b32 v70, v79, s20, v16
	global_store_dwordx4 v[14:15], v[70:73], off
	v_lshl_add_u64 v[14:15], v[14:15], 0, s[8:9]
	s_cbranch_scc0 .LBB0_1370
; __device__ __forceinline__ int mk_lane() { int l_ = (int)__builtin_amdgcn_mbcnt_hi(~0u, __builtin_amdgcn_mbcnt_lo(~0u, 0u)); asm volatile("" : "+v"(l_)); return l_; }
; #define BOTH(k) (IN(k) && IN((k) + 1))
; __device__ __forceinline__ void xcd_barrier_complete(unsigned* bar, unsigned x, unsigned& nloc, unsigned& nx) {
;     const unsigned G = gridDim.x * gridDim.y * gridDim.z;
;     unsigned sum, cnt, mine, sp = 0u;
;     for (;;) {
;         sum = 0u; cnt = 0u; mine = 0u;
; #pragma unroll
;         for (unsigned j = 0; j < 16; ++j) { const unsigned c = xb_ld(&bar[XB_XCNT(j)]); sum += c; cnt += (c > 0u) ? 1u : 0u; mine = (j == x) ? c : mine; }
;         if (sum == G) break;
;         __builtin_amdgcn_s_sleep(1);
;         if ((++sp & 255u) == 0u) { if (xb_ld(&bar[XB_TMO])) break; if (sp > XB_SPIN_CAP) { atomicAdd(&bar[XB_TMO], 1u); break; } }
;     }
;     nloc = mine > 0u ? mine : 1u; nx = cnt > 0u ? cnt : 1u;
; }
; __device__ __forceinline__ void xcd_barrier(const XcdBarrier& b, int wave_id, int pair = -1) {
;     asm volatile("s_waitcnt vmcnt(0)" ::: "memory");
;     __syncthreads();
;     if (wave_id == 0 && mk_lane() == 0) {
;         unsigned* bar = b.bar;
;         __builtin_amdgcn_s_waitcnt(0);
;         unsigned nloc = b.st[0], nx = b.st[1];
;         if (nloc == 0u) { xcd_barrier_complete(bar, b.x, nloc, nx); b.st[0] = nloc; b.st[1] = nx; }
; template <int K> __device__ __forceinline__ void run_phase(Frame& F, const XcdBarrier& bar, int lo, int hi, unsigned char* lds) {
;     ...
;         if (BOTH(k)) {
;             constexpr bool LOCAL_SEAM = MK_LOCALBAR && (sub == 2 || (sub == 6 && l == 0));
;             bool local = false;
;             if (LOCAL_SEAM) local = __hip_atomic_load((unsigned*)(F.ctl + CW_LBAR + 24 * 64), __ATOMIC_RELAXED, __HIP_MEMORY_SCOPE_AGENT) == 0u;
;             constexpr bool PAIR_SEAM = MK_LOCALBAR && (sub == 0 || sub == 1);
;             bool pairok = false;
;             if (PAIR_SEAM) pairok = __hip_atomic_load((unsigned*)(F.ctl + CW_LBAR + 24 * 64), __ATOMIC_RELAXED, __HIP_MEMORY_SCOPE_AGENT) == 0u;
;             if (local) xcd_local_barrier((unsigned*)(F.ctl + CW_LBAR + ((sub == 2 ? l : 2) * 8 + (bx & 7)) * 64), (unsigned)(G >> 3), (unsigned*)(F.ctl + CW_BAR) + XB_TMO, F.wave);
;             else xcd_barrier(bar, F.wave, pairok ? ((bx & 7) >> 1) : -1);
	s_mov_b32 s21, 32
	s_mov_b64 s[6:7], 0
	s_and_b64 vcc, exec, s[10:11]
	s_cbranch_vccz .LBB0_1364
	s_cmp_lt_i32 s41, 11
	s_barrier
	s_cbranch_scc1 .LBB0_1429
	v_mov_b32_e32 v0, 0x31000
	global_load_dword v0, v0, s[30:31] offset:2048 sc1
	s_waitcnt vmcnt(0)
	s_andn2_b64 vcc, exec, s[38:39]
	s_barrier
	s_cbranch_vccnz .LBB0_1428
	s_nop 0
	v_cmp_eq_u32_e32 vcc, 0, v194
	s_and_saveexec_b64 s[6:7], vcc
	s_cbranch_execz .LBB0_1427
	s_add_i32 s4, 0, 0x27f60
	v_mov_b32_e32 v1, s4
	s_waitcnt vmcnt(0) expcnt(0) lgkmcnt(0)
	ds_read_b32 v3, v1
	s_add_i32 s4, 0, 0x27f64
	v_mov_b32_e32 v1, s4
	ds_read_b32 v1, v1
	s_waitcnt lgkmcnt(1)
	v_cmp_ne_u32_e32 vcc, 0, v3
	s_cbranch_vccnz .LBB0_1391
	v_readlane_b32 s4, v248, 0
	v_readlane_b32 s5, v248, 1
	s_load_dwordx2 s[10:11], s[4:5], 0x4
	s_add_u32 s4, s30, 0x4200
	s_addc_u32 s5, s31, 0
	s_add_u32 s8, s30, 0x4400
	s_addc_u32 s9, s31, 0
	s_waitcnt lgkmcnt(0)
	s_mul_i32 s58, s10, s60
	s_add_u32 s10, s30, 0x4500
	s_mul_i32 s58, s58, s11
	s_addc_u32 s11, s31, 0
	s_add_u32 s12, s30, 0x4600
	s_addc_u32 s13, s31, 0
	s_add_u32 s14, s30, 0x4700
	s_addc_u32 s15, s31, 0
	s_add_u32 s16, s30, 0x4800
	s_addc_u32 s17, s31, 0
	s_add_u32 s18, s30, 0x4900
	s_addc_u32 s19, s31, 0
	s_add_u32 s20, s30, 0x4a00
	s_addc_u32 s21, s31, 0
	s_add_u32 s22, s30, 0x4b00
	s_addc_u32 s23, s31, 0
	s_add_u32 s24, s30, 0x4c00
	s_addc_u32 s25, s31, 0
	s_add_u32 s26, s30, 0x4d00
	s_addc_u32 s27, s31, 0
	s_add_u32 s28, s30, 0x4e00
	s_addc_u32 s29, s31, 0
	s_add_u32 s42, s30, 0x4f00
	s_addc_u32 s43, s31, 0
	s_add_u32 s44, s30, 0x5000
	s_addc_u32 s45, s31, 0
	s_add_u32 s46, s30, 0x5100
	s_addc_u32 s47, s31, 0
	s_add_u32 s48, s30, 0x5200
	s_addc_u32 s49, s31, 0
	s_add_u32 s50, s30, 0x5300
	s_addc_u32 s51, s31, 0
	s_mov_b32 s59, 1
	v_mov_b32_e32 v17, 0
	s_branch .LBB0_1378

; #define LAS __attribute__((address_space(3)))
; __device__ __forceinline__ void peer_ln2_phase(LAS unsigned char* lds, int wave, int blk, const bf16* __restrict__ X1B, const bf16* __restrict__ YT, const float* __restrict__ g2, const float* __restrict__ b2, ...
;     ...
;     for (int i = 0; i < 8; ++i) {
;         const int tk = wave * 8 + i; const size_t t = (size_t)blk * 64 + tk;
;         float z[16]; float s = 0.f;
; #pragma unroll
;         for (int k = 0; k < 16; ++k) { const float xv = __uint_as_float((unsigned)__builtin_nontemporal_load((const unsigned short*)X1B + t * 1024 + lane + 64 * k) << 16); const unsigned yb = *(const LAS unsigned short*)(lds + (lane + 64 * k) * 136 + tk * 2);
;             z[k] = 1.41421356237309515f * xv + __uint_as_float(yb << 16); s += z[k]; }
; #pragma unroll
;         for (int o = 1; o < 64; o <<= 1) s += __shfl_xor(s, o);
;         const float mean = s * (1.0f / 1024.0f); float sq = 0.f;
; #pragma unroll
;         for (int k = 0; k < 16; ++k) { z[k] -= mean; sq += z[k] * z[k]; }
; #pragma unroll
;         for (int o = 1; o < 64; o <<= 1) sq += __shfl_xor(sq, o);
.LBB0_2023:
	global_load_ushort v60, v[0:1], off offset:-1024 nt
	global_load_ushort v61, v[0:1], off offset:-896 nt
	global_load_ushort v62, v[0:1], off offset:-768 nt
	s_waitcnt lgkmcnt(0)
	global_load_ushort v63, v[0:1], off offset:-640 nt
	global_load_ushort v64, v[0:1], off offset:-512 nt
	global_load_ushort v65, v[0:1], off offset:-384 nt
	global_load_ushort v66, v[0:1], off offset:-256 nt
	global_load_ushort v67, v[0:1], off offset:-128 nt
	global_load_ushort v68, v[0:1], off nt
	global_load_ushort v69, v[0:1], off offset:128 nt
	global_load_ushort v70, v[0:1], off offset:256 nt
	global_load_ushort v71, v[0:1], off offset:384 nt
	global_load_ushort v72, v[0:1], off offset:512 nt
	global_load_ushort v73, v[0:1], off offset:640 nt
	global_load_ushort v74, v[0:1], off offset:768 nt
	global_load_ushort v75, v[0:1], off offset:896 nt
	v_add_u32_e32 v52, 0xffffbc00, v43
	v_add_u32_e32 v46, 0xfffef000, v43
	v_add_u32_e32 v47, 0xffff1200, v43
	v_add_u32_e32 v48, 0xffff3400, v43
	v_add_u32_e32 v49, 0xffff5600, v43
	v_add_u32_e32 v50, 0xffff7800, v43
	v_add_u32_e32 v51, 0xffff9a00, v43
	v_add_u32_e32 v53, 0xffffde00, v43
	ds_read_u16 v54, v43
	ds_read_u16 v55, v43 offset:8704
	ds_read_u16 v56, v43 offset:17408
	ds_read_u16 v57, v43 offset:26112
	ds_read_u16 v58, v43 offset:34816
	ds_read_u16 v59, v43 offset:43520
	ds_read_u16 v76, v43 offset:52224
	ds_read_u16 v77, v43 offset:60928
	ds_read_u16 v78, v46
	ds_read_u16 v79, v47
	ds_read_u16 v80, v48
	ds_read_u16 v81, v49
	ds_read_u16 v82, v50
	ds_read_u16 v83, v51
	ds_read_u16 v52, v52
	ds_read_u16 v84, v53
	s_waitcnt lgkmcnt(10)
	v_lshlrev_b32_e32 v46, 16, v59
	s_waitcnt lgkmcnt(7)
	v_lshlrev_b32_e32 v59, 16, v78
	v_lshlrev_b32_e32 v47, 16, v58
	s_waitcnt lgkmcnt(6)
	v_lshlrev_b32_e32 v58, 16, v79
	v_lshlrev_b32_e32 v48, 16, v57
	s_waitcnt lgkmcnt(5)
	v_lshlrev_b32_e32 v57, 16, v80
	v_lshlrev_b32_e32 v49, 16, v56
	s_waitcnt lgkmcnt(4)
	v_lshlrev_b32_e32 v56, 16, v81
	v_lshlrev_b32_e32 v50, 16, v55
	s_waitcnt lgkmcnt(3)
	v_lshlrev_b32_e32 v55, 16, v82
	v_lshlrev_b32_e32 v51, 16, v54
	s_waitcnt lgkmcnt(2)
	v_lshlrev_b32_e32 v54, 16, v83
	s_waitcnt lgkmcnt(1)
	v_lshlrev_b32_e32 v53, 16, v52
	s_waitcnt lgkmcnt(0)
	v_lshlrev_b32_e32 v52, 16, v84
	s_andn2_b64 vcc, exec, s[6:7]
	s_waitcnt vmcnt(15)
	v_lshlrev_b32_e32 v60, 16, v60
	s_waitcnt vmcnt(14)
	v_lshlrev_b32_e32 v61, 16, v61
	v_fmac_f32_e32 v59, 0x3fb504f3, v60
	s_waitcnt vmcnt(13)
	v_lshlrev_b32_e32 v62, 16, v62
	v_fmac_f32_e32 v58, 0x3fb504f3, v61
	v_add_f32_e32 v60, 0, v59
	s_waitcnt vmcnt(12)
	v_lshlrev_b32_e32 v63, 16, v63
	v_fmac_f32_e32 v57, 0x3fb504f3, v62
	v_add_f32_e32 v60, v60, v58
	s_waitcnt vmcnt(11)
	v_lshlrev_b32_e32 v64, 16, v64
	v_fmac_f32_e32 v56, 0x3fb504f3, v63
	v_add_f32_e32 v60, v60, v57
	s_waitcnt vmcnt(10)
	v_lshlrev_b32_e32 v65, 16, v65
	v_fmac_f32_e32 v55, 0x3fb504f3, v64
	v_add_f32_e32 v60, v60, v56
	s_waitcnt vmcnt(9)
	v_lshlrev_b32_e32 v66, 16, v66
	v_fmac_f32_e32 v54, 0x3fb504f3, v65
	v_add_f32_e32 v60, v60, v55
	s_waitcnt vmcnt(8)
	v_lshlrev_b32_e32 v67, 16, v67
	v_fmac_f32_e32 v53, 0x3fb504f3, v66
	v_add_f32_e32 v60, v60, v54
	s_waitcnt vmcnt(7)
	v_lshlrev_b32_e32 v68, 16, v68
	v_fmac_f32_e32 v52, 0x3fb504f3, v67
	v_add_f32_e32 v60, v60, v53
	s_waitcnt vmcnt(6)
	v_lshlrev_b32_e32 v69, 16, v69
	v_fmac_f32_e32 v51, 0x3fb504f3, v68
	v_add_f32_e32 v60, v60, v52
	s_waitcnt vmcnt(5)
	v_lshlrev_b32_e32 v70, 16, v70
	v_fmac_f32_e32 v50, 0x3fb504f3, v69
	v_add_f32_e32 v60, v60, v51
	s_waitcnt vmcnt(4)
	v_lshlrev_b32_e32 v71, 16, v71
	v_fmac_f32_e32 v49, 0x3fb504f3, v70
	v_add_f32_e32 v60, v60, v50
	s_waitcnt vmcnt(3)
	v_lshlrev_b32_e32 v72, 16, v72
	v_fmac_f32_e32 v48, 0x3fb504f3, v71
	v_add_f32_e32 v60, v60, v49
	s_waitcnt vmcnt(2)
	v_lshlrev_b32_e32 v73, 16, v73
	v_fmac_f32_e32 v47, 0x3fb504f3, v72
	v_add_f32_e32 v60, v60, v48
	v_fmac_f32_e32 v46, 0x3fb504f3, v73
	v_add_f32_e32 v60, v60, v47
	v_add_f32_e32 v61, v60, v46
	s_waitcnt vmcnt(1)
	v_lshlrev_b32_e32 v62, 16, v74
	v_lshlrev_b32_e32 v60, 16, v76
	v_fmac_f32_e32 v60, 0x3fb504f3, v62
	v_add_f32_e32 v62, v61, v60
	s_waitcnt vmcnt(0)
	v_lshlrev_b32_e32 v63, 16, v75
	v_lshlrev_b32_e32 v61, 16, v77
	v_fmac_f32_e32 v61, 0x3fb504f3, v63
	v_add_f32_e32 v62, v62, v61
	s_nop 1
	v_add_f32_dpp v62, v62, v62 row_shr:1 row_mask:0xf bank_mask:0xf
	s_nop 1
	v_add_f32_dpp v62, v62, v62 row_shr:2 row_mask:0xf bank_mask:0xf
	s_nop 1
	v_add_f32_dpp v62, v62, v62 row_shr:4 row_mask:0xf bank_mask:0xf
	s_nop 1
	v_add_f32_dpp v62, v62, v62 row_shr:8 row_mask:0xf bank_mask:0xf
	s_nop 1
	v_add_f32_dpp v62, v62, v62 row_bcast:15 row_mask:0xa bank_mask:0xf
	s_nop 1
	v_add_f32_dpp v62, v62, v62 row_bcast:31 row_mask:0xc bank_mask:0xf
	s_nop 1
	v_readlane_b32 s98, v62, 63
	s_nop 1
	v_mov_b32_e32 v62, s98
	v_fmac_f32_e32 v58, 0xba800000, v62
	v_fmac_f32_e32 v59, 0xba800000, v62
	v_mul_f32_e32 v63, v58, v58
	v_fmac_f32_e32 v57, 0xba800000, v62
	v_fmac_f32_e32 v63, v59, v59
	v_fmac_f32_e32 v56, 0xba800000, v62
	v_fmac_f32_e32 v63, v57, v57
	v_fmac_f32_e32 v55, 0xba800000, v62
	v_fmac_f32_e32 v63, v56, v56
	v_fmac_f32_e32 v54, 0xba800000, v62
	v_fmac_f32_e32 v63, v55, v55
	v_fmac_f32_e32 v53, 0xba800000, v62
	v_fmac_f32_e32 v63, v54, v54
	v_fmac_f32_e32 v52, 0xba800000, v62
	v_fmac_f32_e32 v63, v53, v53
	v_fmac_f32_e32 v51, 0xba800000, v62
	v_fmac_f32_e32 v63, v52, v52
	v_fmac_f32_e32 v50, 0xba800000, v62
	v_fmac_f32_e32 v63, v51, v51
	v_fmac_f32_e32 v49, 0xba800000, v62
	v_fmac_f32_e32 v63, v50, v50
	v_fmac_f32_e32 v48, 0xba800000, v62
	v_fmac_f32_e32 v63, v49, v49
	v_fmac_f32_e32 v47, 0xba800000, v62
	v_fmac_f32_e32 v63, v48, v48
	v_fmac_f32_e32 v46, 0xba800000, v62
	v_fmac_f32_e32 v63, v47, v47
	v_fmac_f32_e32 v60, 0xba800000, v62
	v_fmac_f32_e32 v63, v46, v46
	v_fmac_f32_e32 v63, v60, v60
	v_fmac_f32_e32 v61, 0xba800000, v62
	v_fmac_f32_e32 v63, v61, v61
	ds_bpermute_b32 v62, v37, v63
	s_waitcnt lgkmcnt(0)
	v_add_f32_e32 v62, v63, v62
	ds_bpermute_b32 v63, v38, v62
	s_waitcnt lgkmcnt(0)
	v_add_f32_e32 v62, v62, v63
	ds_bpermute_b32 v63, v39, v62
	s_waitcnt lgkmcnt(0)
	v_add_f32_e32 v62, v62, v63
	ds_bpermute_b32 v63, v40, v62
	s_waitcnt lgkmcnt(0)
	v_add_f32_e32 v62, v62, v63
	ds_bpermute_b32 v63, v41, v62
	s_waitcnt lgkmcnt(0)
	v_add_f32_e32 v62, v62, v63
	ds_bpermute_b32 v63, v42, v62
	s_cbranch_vccnz .LBB0_2022
; __device__ __forceinline__ void peer_ln2_phase(LAS unsigned char* lds, int wave, int blk, const bf16* __restrict__ X1B, const bf16* __restrict__ YT, const float* __restrict__ g2, const float* __restrict__ b2, ...
;     ...
;         for (int o = 1; o < 64; o <<= 1) sq += __shfl_xor(sq, o);
;         const float rstd = 1.0f / sqrtf(sq * (1.0f / 1024.0f) + 1e-5f);
; #pragma unroll
;         for (int k = 0; k < 16; ++k) { z[k] = z[k] * rstd * gv[k] + bv[k]; if (outf) __builtin_nontemporal_store(z[k], outf + t * 1024 + lane + 64 * k); }
	s_waitcnt lgkmcnt(0)
	v_add_f32_e32 v62, v62, v63
	v_fmamk_f32 v62, v62, 0x3a800000, v44
	v_mul_f32_e32 v63, 0x4f800000, v62
	v_cmp_gt_f32_e32 vcc, s8, v62
	s_nop 1
	v_cndmask_b32_e32 v62, v62, v63, vcc
	v_sqrt_f32_e32 v63, v62
	s_nop 0
	v_add_u32_e32 v64, -1, v63
	v_fma_f32 v66, -v64, v63, v62
	v_add_u32_e32 v65, 1, v63
	v_cmp_ge_f32_e64 s[0:1], 0, v66
	s_nop 1
	v_cndmask_b32_e64 v64, v63, v64, s[0:1]
	v_fma_f32 v63, -v65, v63, v62
	v_cmp_lt_f32_e64 s[0:1], 0, v63
	s_nop 1
	v_cndmask_b32_e64 v63, v64, v65, s[0:1]
	v_mul_f32_e32 v64, 0x37800000, v63
	v_cndmask_b32_e32 v63, v63, v64, vcc
	v_cmp_class_f32_e32 vcc, v62, v45
	s_nop 1
	v_cndmask_b32_e32 v64, v63, v62, vcc
	v_div_scale_f32 v65, s[0:1], v64, v64, 1.0
	v_rcp_f32_e32 v66, v65
	v_lshl_add_u64 v[62:63], v[2:3], 0, s[4:5]
	v_fma_f32 v67, -v65, v66, 1.0
	v_fmac_f32_e32 v66, v67, v66
	v_div_scale_f32 v67, vcc, 1.0, v64, 1.0
	v_mul_f32_e32 v68, v67, v66
	v_fma_f32 v69, -v65, v68, v67
	v_fmac_f32_e32 v68, v69, v66
	v_fma_f32 v65, -v65, v68, v67
	v_div_fmas_f32 v65, v65, v66, v68
	v_div_fixup_f32 v64, v65, v64, 1.0
	v_mul_f32_e32 v46, v46, v64
	v_fma_f32 v46, v26, v46, v34
	global_store_dword v[62:63], v46, off offset:3328 nt
	v_mul_f32_e32 v46, v60, v64
	v_fma_f32 v46, v27, v46, v35
	v_mul_f32_e32 v59, v59, v64
	v_mul_f32_e32 v58, v58, v64
	v_mul_f32_e32 v57, v57, v64
	v_mul_f32_e32 v56, v56, v64
	v_mul_f32_e32 v55, v55, v64
	v_mul_f32_e32 v54, v54, v64
	v_mul_f32_e32 v53, v53, v64
	v_mul_f32_e32 v52, v52, v64
	v_mul_f32_e32 v51, v51, v64
	v_mul_f32_e32 v50, v50, v64
	v_mul_f32_e32 v49, v49, v64
	v_mul_f32_e32 v48, v48, v64
	v_mul_f32_e32 v47, v47, v64
	global_store_dword v[62:63], v46, off offset:3584 nt
	v_mul_f32_e32 v46, v61, v64
	v_fma_f32 v59, v21, v59, v29
	v_fma_f32 v58, v4, v58, v13
	v_fma_f32 v57, v5, v57, v14
	v_fma_f32 v56, v6, v56, v15
	v_fma_f32 v55, v7, v55, v16
	v_fma_f32 v54, v9, v54, v17
	v_fma_f32 v53, v10, v53, v18
	v_fma_f32 v52, v11, v52, v19
	v_fma_f32 v51, v12, v51, v20
	v_fma_f32 v50, v22, v50, v30
	v_fma_f32 v49, v23, v49, v31
	v_fma_f32 v48, v24, v48, v32
	v_fma_f32 v47, v25, v47, v33
	v_fma_f32 v46, v28, v46, v36
	global_store_dword v[62:63], v59, off nt
	global_store_dword v[62:63], v58, off offset:256 nt
	global_store_dword v[62:63], v57, off offset:512 nt
	global_store_dword v[62:63], v56, off offset:768 nt
	global_store_dword v[62:63], v55, off offset:1024 nt
	global_store_dword v[62:63], v54, off offset:1280 nt
	global_store_dword v[62:63], v53, off offset:1536 nt
	global_store_dword v[62:63], v52, off offset:1792 nt
	global_store_dword v[62:63], v51, off offset:2048 nt
	global_store_dword v[62:63], v50, off offset:2304 nt
	global_store_dword v[62:63], v49, off offset:2560 nt
	global_store_dword v[62:63], v48, off offset:2816 nt
	global_store_dword v[62:63], v47, off offset:3072 nt
	global_store_dword v[62:63], v46, off offset:3840 nt
	s_branch .LBB0_2022
